# speedup vs baseline: 1.0341x; 1.0058x over previous
.LBB0_23:
	s_or_b64 exec, exec, s[8:9]
	v_mov_b32_e32 v43, 0
	s_waitcnt lgkmcnt(0)
	s_barrier
	s_and_saveexec_b64 s[8:9], s[4:5]
	ds_read_b32 v43, v1
	s_or_b64 exec, exec, s[8:9]
	s_waitcnt lgkmcnt(0)
	v_add_u32_dpp v26, v43, v43 row_shr:1 row_mask:0xf bank_mask:0xf bound_ctrl:1
	v_and_b32_e32 v34, 63, v0
	v_cmp_eq_u32_e64 s[8:9], 63, v34
	v_add_u32_dpp v26, v26, v26 row_shr:2 row_mask:0xf bank_mask:0xf bound_ctrl:1
	s_nop 1
	v_add_u32_dpp v26, v26, v26 row_shr:4 row_mask:0xf bank_mask:0xf bound_ctrl:1
	s_nop 1
	v_add_u32_dpp v44, v26, v26 row_shr:8 row_mask:0xf bank_mask:0xf bound_ctrl:1
	s_nop 1
	v_add_u32_dpp v44, v44, v44 row_bcast:15 row_mask:0xa bank_mask:0xf
	s_nop 1
	v_add_u32_dpp v44, v44, v44 row_bcast:31 row_mask:0xc bank_mask:0xf
	s_and_saveexec_b64 s[12:13], s[8:9]
	s_xor_b64 s[8:9], exec, s[12:13]
	v_lshrrev_b32_e32 v26, 4, v0
	v_and_b32_e32 v26, 28, v26
	ds_write_b32 v26, v44 offset:3132
	s_or_b64 exec, exec, s[8:9]
	v_mov_b32_e32 v26, 0xc3c
	v_mov_b32_e32 v27, 0xc44
	v_mov_b32_e32 v28, 0xc4c
	s_waitcnt lgkmcnt(0)
	s_barrier
	v_mov_b32_e32 v45, 0xc54
	ds_read2_b32 v[32:33], v26 offset1:1
	ds_read2_b32 v[30:31], v27 offset1:1
	ds_read2_b32 v[28:29], v28 offset1:1
	ds_read2_b32 v[26:27], v45 offset1:1
	s_waitcnt lgkmcnt(0)
	s_and_saveexec_b64 s[8:9], s[4:5]
	s_cbranch_execz .LBB0_29
	v_cmp_lt_u32_e64 s[4:5], 63, v0
	v_sub_u32_e32 v43, v44, v43
	s_nop 0
	v_cndmask_b32_e64 v44, 0, v32, s[4:5]
	s_movk_i32 s4, 0x7f
	v_cmp_lt_u32_e64 s[4:5], s4, v0
	s_nop 1
	v_cndmask_b32_e64 v45, 0, v33, s[4:5]
	s_movk_i32 s4, 0xbf
	v_cmp_lt_u32_e64 s[4:5], s4, v0
	v_add3_u32 v43, v43, v44, v45
	s_nop 0
	v_cndmask_b32_e64 v44, 0, v30, s[4:5]
	s_movk_i32 s4, 0xff
	v_cmp_lt_u32_e64 s[4:5], s4, v0
	s_nop 1
	v_cndmask_b32_e64 v45, 0, v31, s[4:5]
	s_movk_i32 s4, 0x13f
	v_cmp_lt_u32_e64 s[4:5], s4, v0
	v_add3_u32 v43, v43, v44, v45
	s_nop 0
	v_cndmask_b32_e64 v44, 0, v28, s[4:5]
	s_movk_i32 s4, 0x17f
	v_cmp_lt_u32_e64 s[4:5], s4, v0
	s_nop 1
	v_cndmask_b32_e64 v45, 0, v29, s[4:5]
	v_add3_u32 v43, v43, v44, v45
	ds_write_b32 v1, v43 offset:1564

.LBB0_31:
	s_or_b64 exec, exec, s[8:9]
	s_movk_i32 s4, 0x188
	v_cmp_gt_u32_e64 s[4:5], s4, v0
	s_waitcnt vmcnt(0) lgkmcnt(0)
	s_barrier
	s_and_saveexec_b64 s[8:9], s[4:5]
	s_cbranch_execnz .LBB0_47
	s_or_b64 exec, exec, s[8:9]
	s_load_dwordx2 s[4:5], s[0:1], 0x20
	s_and_saveexec_b64 s[8:9], s[6:7]
	s_cbranch_execnz .LBB0_48

.LBB0_34:
	v_ashrrev_i32_e32 v1, 8, v6
	v_ashrrev_i32_e32 v26, 8, v7
	v_ashrrev_i32_e32 v27, 8, v8
	v_ashrrev_i32_e32 v28, 8, v9
	v_lshlrev_b32_e32 v1, 2, v1
	v_lshlrev_b32_e32 v26, 2, v26
	v_lshlrev_b32_e32 v27, 2, v27
	v_lshlrev_b32_e32 v28, 2, v28
	ds_read_b32 v1, v1 offset:1564
	ds_read_b32 v26, v26 offset:1564
	ds_read_b32 v27, v27 offset:1564
	ds_read_b32 v28, v28 offset:1564
	s_mov_b32 s8, 0x1fe0000
	v_lshlrev_b32_e32 v6, 17, v6
	v_lshlrev_b32_e32 v7, 17, v7
	v_lshlrev_b32_e32 v8, 17, v8
	v_lshlrev_b32_e32 v9, 17, v9
	v_and_or_b32 v6, v6, s8, v10
	v_and_or_b32 v7, v7, s8, v11
	v_and_or_b32 v8, v8, s8, v12
	v_and_or_b32 v9, v9, s8, v13
	v_lshlrev_b32_e32 v41, 3, v41
	v_lshlrev_b32_e32 v37, 3, v37
	v_lshlrev_b32_e32 v42, 3, v42
	v_lshlrev_b32_e32 v39, 3, v39
	v_mov_b32_e32 v31, v2
	v_mov_b32_e32 v33, v4
	v_mov_b32_e32 v30, v6
	v_mov_b32_e32 v32, v8
	v_mov_b32_e32 v2, v7
	v_mov_b32_e32 v4, v9
	s_waitcnt lgkmcnt(3)
	v_lshl_add_u32 v1, v1, 3, v41
	s_waitcnt lgkmcnt(2)
	v_lshl_add_u32 v26, v26, 3, v37
	s_waitcnt lgkmcnt(1)
	v_lshl_add_u32 v27, v27, 3, v42
	s_waitcnt lgkmcnt(0)
	v_lshl_add_u32 v28, v28, 3, v39
	ds_write_b64 v1, v[30:31] offset:8192
	ds_write_b64 v26, v[2:3] offset:8192
	ds_write_b64 v27, v[32:33] offset:8192
	ds_write_b64 v28, v[4:5] offset:8192
.LBB0_35:
	s_or_b64 exec, exec, s[6:7]
	v_lshlrev_b32_e32 v1, 3, v0
	s_waitcnt lgkmcnt(0)
	s_barrier
	ds_read_b64 v[4:5], v1 offset:8192
	ds_read_b64 v[6:7], v1 offset:12288
	ds_read_b64 v[8:9], v1 offset:16384
	ds_read_b64 v[10:11], v1 offset:20480
	ds_read_b64 v[12:13], v1 offset:24576
	ds_read_b64 v[14:15], v1 offset:28672
	ds_read_b64 v[16:17], v1 offset:32768
	ds_read_b64 v[18:19], v1 offset:36864
	v_add_u32_e32 v2, s10, v0
	v_lshlrev_b32_e32 v2, 3, v2
	v_add_u32_e32 v20, 0x1000, v2
	v_add_u32_e32 v21, 0x2000, v2
	v_add_u32_e32 v22, 0x3000, v2
	v_add_u32_e32 v23, 0x4000, v2
	v_add_u32_e32 v24, 0x5000, v2
	v_add_u32_e32 v25, 0x6000, v2
	v_add_u32_e32 v26, 0x7000, v2
	s_waitcnt lgkmcnt(7)
	global_store_dwordx2 v2, v[4:5], s[4:5]
	s_mov_b64 s[6:7], exec
	v_or_b32_e32 v3, 0x200, v0
	v_cmp_gt_u32_e32 vcc, s3, v3
	s_and_b64 exec, exec, vcc
	s_cbranch_execz .LBB0_43
	s_waitcnt lgkmcnt(6)
	global_store_dwordx2 v20, v[6:7], s[4:5]
	v_or_b32_e32 v3, 0x400, v0
	v_cmp_gt_u32_e32 vcc, s3, v3
	s_and_b64 exec, exec, vcc
	s_cbranch_execz .LBB0_43
	s_waitcnt lgkmcnt(5)
	global_store_dwordx2 v21, v[8:9], s[4:5]
	v_or_b32_e32 v3, 0x600, v0
	v_cmp_gt_u32_e32 vcc, s3, v3
	s_and_b64 exec, exec, vcc
	s_cbranch_execz .LBB0_43
	s_waitcnt lgkmcnt(4)
	global_store_dwordx2 v22, v[10:11], s[4:5]
	v_or_b32_e32 v3, 0x800, v0
	v_cmp_gt_u32_e32 vcc, s3, v3
	s_and_b64 exec, exec, vcc
	s_cbranch_execz .LBB0_43
	s_waitcnt lgkmcnt(3)
	global_store_dwordx2 v23, v[12:13], s[4:5]
	v_or_b32_e32 v3, 0xa00, v0
	v_cmp_gt_u32_e32 vcc, s3, v3
	s_and_b64 exec, exec, vcc
	s_cbranch_execz .LBB0_43
	s_waitcnt lgkmcnt(2)
	global_store_dwordx2 v24, v[14:15], s[4:5]
	v_or_b32_e32 v3, 0xc00, v0
	v_cmp_gt_u32_e32 vcc, s3, v3
	s_and_b64 exec, exec, vcc
	s_cbranch_execz .LBB0_43
	s_waitcnt lgkmcnt(1)
	global_store_dwordx2 v25, v[16:17], s[4:5]
	v_or_b32_e32 v3, 0xe00, v0
	v_cmp_gt_u32_e32 vcc, s3, v3
	s_and_b64 exec, exec, vcc
	s_cbranch_execz .LBB0_43
	s_waitcnt lgkmcnt(0)
	global_store_dwordx2 v26, v[18:19], s[4:5]

.LBB0_48:
	v_ashrrev_i32_e32 v1, 8, v18
	v_ashrrev_i32_e32 v26, 8, v19
	v_ashrrev_i32_e32 v27, 8, v20
	v_ashrrev_i32_e32 v28, 8, v21
	v_lshlrev_b32_e32 v1, 2, v1
	v_lshlrev_b32_e32 v26, 2, v26
	v_lshlrev_b32_e32 v27, 2, v27
	v_lshlrev_b32_e32 v28, 2, v28
	ds_read_b32 v1, v1 offset:1564
	ds_read_b32 v26, v26 offset:1564
	ds_read_b32 v27, v27 offset:1564
	ds_read_b32 v28, v28 offset:1564
	s_mov_b32 s6, 0x1fe0000
	v_lshlrev_b32_e32 v18, 17, v18
	v_lshlrev_b32_e32 v19, 17, v19
	v_lshlrev_b32_e32 v20, 17, v20
	v_lshlrev_b32_e32 v21, 17, v21
	v_and_or_b32 v18, v18, s6, v22
	v_and_or_b32 v19, v19, s6, v23
	v_and_or_b32 v20, v20, s6, v24
	v_and_or_b32 v21, v21, s6, v25
	v_lshlrev_b32_e32 v38, 3, v38
	v_lshlrev_b32_e32 v35, 3, v35
	v_lshlrev_b32_e32 v40, 3, v40
	v_lshlrev_b32_e32 v36, 3, v36
	v_mov_b32_e32 v31, v14
	v_mov_b32_e32 v33, v16
	v_mov_b32_e32 v30, v18
	v_mov_b32_e32 v32, v20
	v_mov_b32_e32 v14, v19
	v_mov_b32_e32 v16, v21
	s_waitcnt lgkmcnt(3)
	v_lshl_add_u32 v1, v1, 3, v38
	s_waitcnt lgkmcnt(2)
	v_lshl_add_u32 v26, v26, 3, v35
	s_waitcnt lgkmcnt(1)
	v_lshl_add_u32 v27, v27, 3, v40
	s_waitcnt lgkmcnt(0)
	v_lshl_add_u32 v28, v28, 3, v36
	ds_write_b64 v1, v[30:31] offset:8192
	ds_write_b64 v26, v[14:15] offset:8192
	ds_write_b64 v27, v[32:33] offset:8192
	ds_write_b64 v28, v[16:17] offset:8192
	s_or_b64 exec, exec, s[8:9]
	s_and_saveexec_b64 s[6:7], vcc
	s_cbranch_execnz .LBB0_34
	s_branch .LBB0_35

_Z5k_midPK15HIP_vector_typeIjLj2EEPKiPiPfPjPDF16_:
	s_load_dwordx2 s[4:5], s[0:1], 0x8
	s_load_dwordx2 s[44:45], s[0:1], 0x28
	s_and_b32 s3, s2, 7
	s_lshr_b32 s2, s2, 3
	s_mul_i32 s35, s3, 49
	s_add_i32 s35, s35, s2
	v_min_u32_e32 v1, 0x186, v0
	s_movk_i32 s2, 0x188
	v_mov_b32_e32 v2, s35
	v_mad_u32_u24 v4, v1, s2, v2
	v_mov_b32_e32 v5, 0
	s_waitcnt lgkmcnt(0)
	v_lshl_add_u64 v[2:3], v[4:5], 2, s[4:5]
	global_load_dwordx2 v[2:3], v[2:3], off
	s_lshl_b32 s46, s35, 8
	v_lshrrev_b32_e32 v72, 3, v0
	v_or_b32_e32 v72, s46, v72
	v_and_b32_e32 v56, 7, v0
	v_lshlrev_b32_e32 v56, 4, v56
	v_min_u32_e32 v60, 0x1869f, v72
	v_lshl_or_b32 v60, v60, 7, v56
	v_add_u32_e32 v64, 64, v72
	v_min_u32_e32 v64, 0x1869f, v64
	v_lshl_or_b32 v64, v64, 7, v56
	v_add_u32_e32 v68, 0x80, v72
	v_min_u32_e32 v68, 0x1869f, v68
	v_lshl_or_b32 v68, v68, 7, v56
	v_add_u32_e32 v72, 0xc0, v72
	v_min_u32_e32 v72, 0x1869f, v72
	v_lshl_or_b32 v72, v72, 7, v56
	global_load_dwordx4 v[60:63], v60, s[44:45]
	global_load_dwordx4 v[64:67], v64, s[44:45]
	global_load_dwordx4 v[68:71], v68, s[44:45]
	global_load_dwordx4 v[56:59], v72, s[44:45]
	s_movk_i32 s2, 0x100
	v_cmp_gt_u32_e64 s[4:5], s2, v0
	v_lshlrev_b32_e32 v1, 2, v0
	s_and_saveexec_b64 s[2:3], s[4:5]
	ds_write_b32 v1, v5 offset:3132
	s_or_b64 exec, exec, s[2:3]
	s_movk_i32 s2, 0x187
	v_cmp_gt_u32_e32 vcc, s2, v0
	s_waitcnt vmcnt(4)
	v_sub_u32_e32 v3, v3, v2
	v_and_b32_e32 v7, 63, v0
	v_cndmask_b32_e32 v6, 0, v2, vcc
	v_cndmask_b32_e32 v4, 0, v3, vcc
	v_lshrrev_b32_e32 v20, 6, v0
	v_add_u32_dpp v6, v6, v6 row_shr:1 row_mask:0xf bank_mask:0xf bound_ctrl:1
	v_add_u32_dpp v4, v4, v4 row_shr:1 row_mask:0xf bank_mask:0xf bound_ctrl:1
	v_cmp_eq_u32_e64 s[6:7], 63, v7
	v_add_u32_dpp v6, v6, v6 row_shr:2 row_mask:0xf bank_mask:0xf bound_ctrl:1
	v_add_u32_dpp v4, v4, v4 row_shr:2 row_mask:0xf bank_mask:0xf bound_ctrl:1
	s_nop 0
	v_add_u32_dpp v6, v6, v6 row_shr:4 row_mask:0xf bank_mask:0xf bound_ctrl:1
	v_add_u32_dpp v4, v4, v4 row_shr:4 row_mask:0xf bank_mask:0xf bound_ctrl:1
	s_nop 0
	v_add_u32_dpp v6, v6, v6 row_shr:8 row_mask:0xf bank_mask:0xf bound_ctrl:1
	v_add_u32_dpp v4, v4, v4 row_shr:8 row_mask:0xf bank_mask:0xf bound_ctrl:1
	s_nop 0
	v_add_u32_dpp v6, v6, v6 row_bcast:15 row_mask:0xa bank_mask:0xf
	v_add_u32_dpp v4, v4, v4 row_bcast:15 row_mask:0xa bank_mask:0xf
	s_nop 0
	v_mov_b32_dpp v5, v6 row_bcast:31 row_mask:0xc bank_mask:0xf
	v_add_u32_dpp v4, v4, v4 row_bcast:31 row_mask:0xc bank_mask:0xf
	s_and_saveexec_b64 s[2:3], s[6:7]
	v_add_u32_e32 v5, v6, v5
	v_lshlrev_b32_e32 v6, 2, v20
	v_add_u32_e32 v6, 0x1000, v6
	ds_write2_b32 v6, v4, v5 offset0:15 offset1:23
	s_or_b64 exec, exec, s[2:3]
	v_mov_b32_e32 v5, 0x1074
	s_waitcnt lgkmcnt(0)
	s_barrier
	ds_read2_b32 v[6:7], v5 offset1:1
	v_mov_b32_e32 v5, 0x106c
	v_mov_b32_e32 v10, 0x1064
	v_mov_b32_e32 v12, 0x105c
	ds_read2_b32 v[8:9], v5 offset1:1
	ds_read2_b32 v[10:11], v10 offset1:1
	ds_read2_b32 v[12:13], v12 offset1:1
	v_mov_b32_e32 v5, 0x1054
	s_waitcnt lgkmcnt(3)
	v_readfirstlane_b32 s36, v7
	v_readfirstlane_b32 s38, v6
	s_waitcnt lgkmcnt(1)
	v_readfirstlane_b32 s42, v10
	s_waitcnt lgkmcnt(0)
	v_readfirstlane_b32 s43, v12
	ds_read2_b32 v[6:7], v5 offset1:1
	v_mov_b32_e32 v5, 0x104c
	v_mov_b32_e32 v10, 0x1044
	v_mov_b32_e32 v12, 0x103c
	v_readfirstlane_b32 s39, v9
	v_readfirstlane_b32 s40, v8
	v_readfirstlane_b32 s41, v11
	v_readfirstlane_b32 s37, v13
	ds_read2_b32 v[8:9], v5 offset1:1
	ds_read2_b32 v[10:11], v10 offset1:1
	ds_read2_b32 v[12:13], v12 offset1:1
	s_waitcnt lgkmcnt(3)
	v_readfirstlane_b32 s10, v7
	v_readfirstlane_b32 s11, v6
	s_waitcnt lgkmcnt(2)
	v_readfirstlane_b32 s12, v9
	v_readfirstlane_b32 s13, v8
	s_waitcnt lgkmcnt(1)
	v_readfirstlane_b32 s14, v11
	v_readfirstlane_b32 s15, v10
	s_waitcnt lgkmcnt(0)
	v_readfirstlane_b32 s16, v13
	v_readfirstlane_b32 s17, v12
	s_and_saveexec_b64 s[2:3], vcc
	s_cbranch_execz .LBB1_6
	s_movk_i32 s8, 0x17f
	v_mov_b32_e32 v5, s12
	v_cmp_lt_u32_e32 vcc, s8, v0
	s_movk_i32 s8, 0x13f
	v_mov_b32_e32 v6, s13
	v_cndmask_b32_e32 v5, 0, v5, vcc
	v_cmp_lt_u32_e32 vcc, s8, v0
	s_movk_i32 s8, 0xff
	v_mov_b32_e32 v7, s14
	v_cndmask_b32_e32 v6, 0, v6, vcc
	v_cmp_lt_u32_e32 vcc, s8, v0
	s_movk_i32 s8, 0xbf
	v_mov_b32_e32 v8, s15
	v_cndmask_b32_e32 v7, 0, v7, vcc
	v_cmp_lt_u32_e32 vcc, s8, v0
	s_movk_i32 s8, 0x7f
	v_mov_b32_e32 v9, s16
	v_cndmask_b32_e32 v8, 0, v8, vcc
	v_cmp_lt_u32_e32 vcc, s8, v0
	v_mov_b32_e32 v10, s17
	v_sub_u32_e32 v3, v4, v3
	v_cndmask_b32_e32 v9, 0, v9, vcc
	v_cmp_lt_u32_e32 vcc, 63, v0
	v_lshl_add_u32 v2, v0, 12, v2
	s_nop 0
	v_cndmask_b32_e32 v10, 0, v10, vcc
	v_add3_u32 v3, v3, v10, v9
	v_add3_u32 v3, v3, v8, v7
	v_add3_u32 v3, v3, v6, v5
	ds_write_b32 v1, v3
	ds_write_b32 v1, v2 offset:1568

.Lmid_fill_done:
	s_mov_b64 exec, s[12:13]
	s_waitcnt lgkmcnt(0)
	s_barrier
	v_min_u32_e32 v30, s10, v0
	v_min_u32_e32 v31, s10, v23
	v_min_u32_e32 v32, s10, v28
	v_min_u32_e32 v33, s10, v22
	v_min_u32_e32 v34, s10, v27
	v_min_u32_e32 v35, s10, v26
	v_min_u32_e32 v36, s10, v25
	v_min_u32_e32 v37, s10, v24
	v_min_u32_e32 v38, s10, v21
	v_lshlrev_b32_e32 v30, 2, v30
	v_lshlrev_b32_e32 v31, 2, v31
	v_lshlrev_b32_e32 v32, 2, v32
	v_lshlrev_b32_e32 v33, 2, v33
	v_lshlrev_b32_e32 v34, 2, v34
	v_lshlrev_b32_e32 v35, 2, v35
	v_lshlrev_b32_e32 v36, 2, v36
	v_lshlrev_b32_e32 v37, 2, v37
	v_lshlrev_b32_e32 v38, 2, v38
	ds_read_b32 v30, v30 offset:8192
	ds_read_b32 v31, v31 offset:8192
	ds_read_b32 v32, v32 offset:8192
	ds_read_b32 v33, v33 offset:8192
	ds_read_b32 v34, v34 offset:8192
	ds_read_b32 v35, v35 offset:8192
	ds_read_b32 v36, v36 offset:8192
	ds_read_b32 v37, v37 offset:8192
	ds_read_b32 v38, v38 offset:8192
	s_cmp_gt_i32 s33, 0
	s_cselect_b64 vcc, -1, 0
	s_waitcnt lgkmcnt(8)
	v_lshlrev_b32_e32 v30, 3, v30
	v_cndmask_b32_e32 v30, 0, v30, vcc
	global_load_dwordx2 v[18:19], v30, s[8:9]
	s_waitcnt lgkmcnt(7)
	v_lshlrev_b32_e32 v31, 3, v31
	v_cndmask_b32_e32 v31, 0, v31, vcc
	global_load_dwordx2 v[16:17], v31, s[8:9]
	s_waitcnt lgkmcnt(6)
	v_lshlrev_b32_e32 v32, 3, v32
	v_cndmask_b32_e32 v32, 0, v32, vcc
	global_load_dwordx2 v[12:13], v32, s[8:9]
	s_waitcnt lgkmcnt(5)
	v_lshlrev_b32_e32 v33, 3, v33
	v_cndmask_b32_e32 v33, 0, v33, vcc
	global_load_dwordx2 v[8:9], v33, s[8:9]
	s_waitcnt lgkmcnt(4)
	v_lshlrev_b32_e32 v34, 3, v34
	v_cndmask_b32_e32 v34, 0, v34, vcc
	global_load_dwordx2 v[14:15], v34, s[8:9]
	s_waitcnt lgkmcnt(3)
	v_lshlrev_b32_e32 v35, 3, v35
	v_cndmask_b32_e32 v35, 0, v35, vcc
	global_load_dwordx2 v[10:11], v35, s[8:9]
	s_waitcnt lgkmcnt(2)
	v_lshlrev_b32_e32 v36, 3, v36
	v_cndmask_b32_e32 v36, 0, v36, vcc
	global_load_dwordx2 v[6:7], v36, s[8:9]
	s_waitcnt lgkmcnt(1)
	v_lshlrev_b32_e32 v37, 3, v37
	v_cndmask_b32_e32 v37, 0, v37, vcc
	global_load_dwordx2 v[4:5], v37, s[8:9]
	s_waitcnt lgkmcnt(0)
	v_lshlrev_b32_e32 v38, 3, v38
	v_cndmask_b32_e32 v38, 0, v38, vcc
	global_load_dwordx2 v[2:3], v38, s[8:9]
	v_mov_b32_e32 v29, 0
	v_cmp_gt_i32_e32 vcc, s33, v0
	v_mov_b32_e32 v34, 0
	s_waitcnt vmcnt(8)
	v_lshrrev_b32_e32 v31, 15, v18
	s_and_saveexec_b64 s[8:9], vcc
	v_and_b32_e32 v30, 0x1fffc, v31
	v_mov_b32_e32 v32, 1
	ds_add_rtn_u32 v34, v30, v32 offset:3132
	s_or_b64 exec, exec, s[8:9]
	v_cmp_gt_i32_e64 s[8:9], s33, v23
	s_waitcnt vmcnt(7)
	v_lshrrev_b32_e32 v30, 15, v16
	s_and_saveexec_b64 s[10:11], s[8:9]
	v_and_b32_e32 v29, 0x1fffc, v30
	v_mov_b32_e32 v32, 1
	ds_add_rtn_u32 v29, v29, v32 offset:3132
	s_or_b64 exec, exec, s[10:11]
	v_cmp_gt_i32_e64 s[10:11], s33, v28
	v_mov_b32_e32 v28, 0
	s_waitcnt vmcnt(6)
	v_lshrrev_b32_e32 v33, 15, v12
	v_mov_b32_e32 v36, 0
	s_and_saveexec_b64 s[12:13], s[10:11]
	v_and_b32_e32 v32, 0x1fffc, v33
	v_mov_b32_e32 v35, 1
	ds_add_rtn_u32 v36, v32, v35 offset:3132
	s_or_b64 exec, exec, s[12:13]
	v_cmp_gt_i32_e64 s[12:13], s33, v22
	s_waitcnt vmcnt(5)
	v_lshrrev_b32_e32 v32, 15, v8
	s_and_saveexec_b64 s[14:15], s[12:13]
	v_and_b32_e32 v28, 0x1fffc, v32
	v_mov_b32_e32 v35, 1
	ds_add_rtn_u32 v28, v28, v35 offset:3132
	s_or_b64 exec, exec, s[14:15]
	v_cmp_gt_i32_e64 s[14:15], s33, v27
	v_mov_b32_e32 v27, 0
	s_waitcnt vmcnt(4)
	v_lshrrev_b32_e32 v35, 15, v14
	v_mov_b32_e32 v38, 0
	s_and_saveexec_b64 s[16:17], s[14:15]
	v_and_b32_e32 v37, 0x1fffc, v35
	v_mov_b32_e32 v38, 1
	ds_add_rtn_u32 v38, v37, v38 offset:3132
	s_or_b64 exec, exec, s[16:17]
	v_cmp_gt_i32_e64 s[16:17], s33, v26
	s_waitcnt vmcnt(3)
	v_lshrrev_b32_e32 v26, 15, v10
	s_and_saveexec_b64 s[18:19], s[16:17]
	v_and_b32_e32 v27, 0x1fffc, v26
	v_mov_b32_e32 v37, 1
	ds_add_rtn_u32 v27, v27, v37 offset:3132
	s_or_b64 exec, exec, s[18:19]
	v_cmp_gt_i32_e64 s[18:19], s33, v25
	v_mov_b32_e32 v25, 0
	s_waitcnt vmcnt(2)
	v_lshrrev_b32_e32 v37, 15, v6
	v_mov_b32_e32 v40, 0
	s_and_saveexec_b64 s[20:21], s[18:19]
	v_and_b32_e32 v39, 0x1fffc, v37
	v_mov_b32_e32 v40, 1
	ds_add_rtn_u32 v40, v39, v40 offset:3132
	s_or_b64 exec, exec, s[20:21]
	v_cmp_gt_i32_e64 s[20:21], s33, v24
	s_waitcnt vmcnt(1)
	v_lshrrev_b32_e32 v24, 15, v4
	s_and_saveexec_b64 s[22:23], s[20:21]
	v_and_b32_e32 v25, 0x1fffc, v24
	v_mov_b32_e32 v39, 1
	ds_add_rtn_u32 v25, v25, v39 offset:3132
	s_or_b64 exec, exec, s[22:23]
	v_cmp_gt_i32_e64 s[22:23], s33, v21
	v_mov_b32_e32 v42, 0
	s_waitcnt vmcnt(0)
	v_lshrrev_b32_e32 v39, 15, v2
	v_mov_b32_e32 v41, 0
	s_and_saveexec_b64 s[30:31], s[22:23]
	v_and_b32_e32 v21, 0x1fffc, v39
	v_mov_b32_e32 v41, 1
	ds_add_rtn_u32 v41, v21, v41 offset:3132
	s_or_b64 exec, exec, s[30:31]
	s_waitcnt lgkmcnt(0)
	s_barrier
	s_and_saveexec_b64 s[30:31], s[4:5]
	ds_read_b32 v42, v1 offset:3132
	s_or_b64 exec, exec, s[30:31]
	s_waitcnt lgkmcnt(0)
	v_add_u32_dpp v21, v42, v42 row_shr:1 row_mask:0xf bank_mask:0xf bound_ctrl:1
	v_mov_b32_e32 v44, 0
	s_nop 0
	v_add_u32_dpp v21, v21, v21 row_shr:2 row_mask:0xf bank_mask:0xf bound_ctrl:1
	s_nop 1
	v_add_u32_dpp v21, v21, v21 row_shr:4 row_mask:0xf bank_mask:0xf bound_ctrl:1
	s_nop 1
	v_add_u32_dpp v43, v21, v21 row_shr:8 row_mask:0xf bank_mask:0xf bound_ctrl:1
	s_nop 1
	v_add_u32_dpp v43, v43, v43 row_bcast:15 row_mask:0xa bank_mask:0xf
	s_nop 1
	v_add_u32_dpp v43, v43, v43 row_bcast:31 row_mask:0xc bank_mask:0xf
	s_and_saveexec_b64 s[30:31], s[6:7]
	v_lshlrev_b32_e32 v20, 2, v20
	ds_write_b32 v20, v43 offset:4156
	s_or_b64 exec, exec, s[30:31]
	v_mov_b32_e32 v20, 0x103c
	s_waitcnt lgkmcnt(0)
	s_barrier
	ds_read2_b32 v[20:21], v20 offset1:1
	ds_read_b32 v44, v44 offset:4164
	s_waitcnt lgkmcnt(0)
	s_and_saveexec_b64 s[6:7], s[4:5]
	s_cbranch_execz .LBB1_60
	s_movk_i32 s4, 0xbf
	v_cmp_lt_u32_e64 s[4:5], s4, v0
	v_sub_u32_e32 v42, v43, v42
	s_nop 0
	v_cndmask_b32_e64 v44, 0, v44, s[4:5]
	s_movk_i32 s4, 0x7f
	v_cmp_lt_u32_e64 s[4:5], s4, v0
	s_nop 1
	v_cndmask_b32_e64 v21, 0, v21, s[4:5]
	v_cmp_lt_u32_e64 s[4:5], 63, v0
	s_nop 1
	v_cndmask_b32_e64 v20, 0, v20, s[4:5]
	v_add_u32_e32 v20, v42, v20
	v_add3_u32 v20, v20, v21, v44
	ds_write_b32 v1, v20 offset:3132
